# P@V: MFMAs of the previous k-step split in two halves, one behind the transposed reads and one behind the image writes (on top of v66)
# speedup vs baseline: 1.0079x; 1.0079x over previous
.LBB0_1334:
	v_and_b32_e32 v34, 64, v209
	v_max_f32_e32 v21, v215, v215
	v_mov_b32_e32 v32, v141
	v_mov_b32_e32 v33, v141
	v_max_f32_e32 v20, v215, v215
	v_readlane_b32 s9, v254, 54
	s_movk_i32 s8, 0x520
	v_lshlrev_b32_e32 v34, 2, v34
	v_permlane16_swap_b32_e32 v20, v21
	s_lshl_b64 s[0:1], s[0:1], 9
	s_lshl_b64 s[0:1], s[0:1], 1
	v_max_f32_e32 v20, v20, v21
	v_mov_b32_e32 v21, v20
	s_nop 1
	v_permlane32_swap_b32_e32 v20, v21
	s_nop 1
	v_max_f32_e32 v20, v20, v21
	v_add_f32_e32 v20, 0xc1000000, v20
	v_pk_add_f32 v[118:119], v[118:119], v[20:21] op_sel_hi:[1,0] neg_lo:[0,1] neg_hi:[0,1]
	v_pk_add_f32 v[120:121], v[120:121], v[20:21] op_sel_hi:[1,0] neg_lo:[0,1] neg_hi:[0,1]
	v_pk_add_f32 v[122:123], v[122:123], v[20:21] op_sel_hi:[1,0] neg_lo:[0,1] neg_hi:[0,1]
	v_pk_add_f32 v[124:125], v[124:125], v[20:21] op_sel_hi:[1,0] neg_lo:[0,1] neg_hi:[0,1]
	v_pk_add_f32 v[126:127], v[126:127], v[20:21] op_sel_hi:[1,0] neg_lo:[0,1] neg_hi:[0,1]
	v_pk_add_f32 v[128:129], v[128:129], v[20:21] op_sel_hi:[1,0] neg_lo:[0,1] neg_hi:[0,1]
	v_pk_add_f32 v[130:131], v[130:131], v[20:21] op_sel_hi:[1,0] neg_lo:[0,1] neg_hi:[0,1]
	v_pk_add_f32 v[132:133], v[132:133], v[20:21] op_sel_hi:[1,0] neg_lo:[0,1] neg_hi:[0,1]
	v_pk_add_f32 v[134:135], v[134:135], v[20:21] op_sel_hi:[1,0] neg_lo:[0,1] neg_hi:[0,1]
	v_pk_add_f32 v[136:137], v[136:137], v[20:21] op_sel_hi:[1,0] neg_lo:[0,1] neg_hi:[0,1]
	v_pk_add_f32 v[156:157], v[156:157], v[20:21] op_sel_hi:[1,0] neg_lo:[0,1] neg_hi:[0,1]
	v_pk_add_f32 v[158:159], v[158:159], v[20:21] op_sel_hi:[1,0] neg_lo:[0,1] neg_hi:[0,1]
	v_pk_add_f32 v[160:161], v[160:161], v[20:21] op_sel_hi:[1,0] neg_lo:[0,1] neg_hi:[0,1]
	v_pk_add_f32 v[162:163], v[162:163], v[20:21] op_sel_hi:[1,0] neg_lo:[0,1] neg_hi:[0,1]
	v_pk_add_f32 v[164:165], v[164:165], v[20:21] op_sel_hi:[1,0] neg_lo:[0,1] neg_hi:[0,1]
	v_pk_add_f32 v[166:167], v[166:167], v[20:21] op_sel_hi:[1,0] neg_lo:[0,1] neg_hi:[0,1]
	v_pk_add_f32 v[168:169], v[168:169], v[20:21] op_sel_hi:[1,0] neg_lo:[0,1] neg_hi:[0,1]
	v_pk_add_f32 v[170:171], v[170:171], v[20:21] op_sel_hi:[1,0] neg_lo:[0,1] neg_hi:[0,1]
	v_pk_add_f32 v[172:173], v[172:173], v[20:21] op_sel_hi:[1,0] neg_lo:[0,1] neg_hi:[0,1]
	v_pk_add_f32 v[174:175], v[174:175], v[20:21] op_sel_hi:[1,0] neg_lo:[0,1] neg_hi:[0,1]
	v_pk_add_f32 v[176:177], v[176:177], v[20:21] op_sel_hi:[1,0] neg_lo:[0,1] neg_hi:[0,1]
	v_pk_add_f32 v[178:179], v[178:179], v[20:21] op_sel_hi:[1,0] neg_lo:[0,1] neg_hi:[0,1]
	v_pk_add_f32 v[180:181], v[180:181], v[20:21] op_sel_hi:[1,0] neg_lo:[0,1] neg_hi:[0,1]
	v_pk_add_f32 v[182:183], v[182:183], v[20:21] op_sel_hi:[1,0] neg_lo:[0,1] neg_hi:[0,1]
	v_pk_add_f32 v[184:185], v[184:185], v[20:21] op_sel_hi:[1,0] neg_lo:[0,1] neg_hi:[0,1]
	v_pk_add_f32 v[186:187], v[186:187], v[20:21] op_sel_hi:[1,0] neg_lo:[0,1] neg_hi:[0,1]
	v_pk_add_f32 v[188:189], v[188:189], v[20:21] op_sel_hi:[1,0] neg_lo:[0,1] neg_hi:[0,1]
	v_pk_add_f32 v[190:191], v[190:191], v[20:21] op_sel_hi:[1,0] neg_lo:[0,1] neg_hi:[0,1]
	v_pk_add_f32 v[192:193], v[192:193], v[20:21] op_sel_hi:[1,0] neg_lo:[0,1] neg_hi:[0,1]
	v_pk_add_f32 v[194:195], v[194:195], v[20:21] op_sel_hi:[1,0] neg_lo:[0,1] neg_hi:[0,1]
	v_pk_add_f32 v[196:197], v[196:197], v[20:21] op_sel_hi:[1,0] neg_lo:[0,1] neg_hi:[0,1]
	v_pk_add_f32 v[198:199], v[198:199], v[20:21] op_sel_hi:[1,0] neg_lo:[0,1] neg_hi:[0,1]
	v_exp_f32_e32 v21, v118
	v_exp_f32_e32 v23, v119
	v_exp_f32_e32 v24, v120
	v_exp_f32_e32 v25, v121
	v_exp_f32_e32 v26, v122
	v_exp_f32_e32 v27, v123
	v_exp_f32_e32 v28, v124
	v_exp_f32_e32 v29, v125
	v_exp_f32_e32 v31, v126
	v_exp_f32_e32 v36, v127
	v_exp_f32_e32 v37, v128
	v_exp_f32_e32 v38, v129
	v_exp_f32_e32 v39, v130
	v_exp_f32_e32 v40, v131
	v_exp_f32_e32 v41, v132
	v_exp_f32_e32 v42, v133
	v_exp_f32_e32 v43, v134
	v_exp_f32_e32 v44, v135
	v_exp_f32_e32 v45, v136
	v_exp_f32_e32 v46, v137
	v_exp_f32_e32 v47, v156
	v_exp_f32_e32 v48, v157
	v_exp_f32_e32 v49, v158
	v_exp_f32_e32 v50, v159
	v_exp_f32_e32 v51, v160
	v_exp_f32_e32 v52, v161
	v_exp_f32_e32 v53, v162
	v_exp_f32_e32 v54, v163
	v_exp_f32_e32 v55, v164
	v_exp_f32_e32 v56, v165
	v_exp_f32_e32 v57, v166
	v_exp_f32_e32 v58, v167
	v_exp_f32_e32 v59, v168
	v_exp_f32_e32 v60, v169
	v_exp_f32_e32 v61, v170
	v_exp_f32_e32 v62, v171
	v_exp_f32_e32 v63, v172
	v_exp_f32_e32 v64, v173
	v_exp_f32_e32 v65, v174
	v_exp_f32_e32 v66, v175
	v_exp_f32_e32 v67, v176
	v_exp_f32_e32 v68, v177
	v_exp_f32_e32 v69, v178
	v_exp_f32_e32 v70, v179
	v_exp_f32_e32 v71, v180
	v_exp_f32_e32 v72, v181
	v_exp_f32_e32 v73, v182
	v_exp_f32_e32 v74, v183
	v_exp_f32_e32 v75, v184
	v_exp_f32_e32 v76, v185
	v_exp_f32_e32 v77, v186
	v_exp_f32_e32 v78, v187
	v_exp_f32_e32 v79, v188
	v_exp_f32_e32 v80, v189
	v_exp_f32_e32 v81, v190
	v_exp_f32_e32 v82, v191
	v_exp_f32_e32 v83, v192
	v_exp_f32_e32 v84, v193
	v_exp_f32_e32 v85, v194
	v_exp_f32_e32 v86, v195
	v_exp_f32_e32 v87, v196
	v_exp_f32_e32 v88, v197
	v_exp_f32_e32 v89, v198
	v_exp_f32_e32 v90, v199
	s_nop 0
	v_pk_add_f32 v[118:119], v[24:25], v[38:39]
	v_pk_add_f32 v[120:121], v[26:27], v[40:41]
	v_pk_add_f32 v[122:123], v[28:29], v[42:43]
	v_pk_add_f32 v[124:125], v[36:37], v[44:45]
	v_pk_add_f32 v[118:119], v[118:119], v[46:47]
	v_pk_add_f32 v[120:121], v[120:121], v[48:49]
	v_pk_add_f32 v[122:123], v[122:123], v[50:51]
	v_pk_add_f32 v[124:125], v[124:125], v[52:53]
	v_pk_add_f32 v[118:119], v[118:119], v[54:55]
	v_pk_add_f32 v[120:121], v[120:121], v[56:57]
	v_pk_add_f32 v[122:123], v[122:123], v[58:59]
	v_pk_add_f32 v[124:125], v[124:125], v[60:61]
	v_pk_add_f32 v[118:119], v[118:119], v[62:63]
	v_pk_add_f32 v[120:121], v[120:121], v[64:65]
	v_pk_add_f32 v[122:123], v[122:123], v[66:67]
	v_pk_add_f32 v[124:125], v[124:125], v[68:69]
	v_pk_add_f32 v[118:119], v[118:119], v[70:71]
	v_pk_add_f32 v[120:121], v[120:121], v[72:73]
	v_pk_add_f32 v[122:123], v[122:123], v[74:75]
	v_pk_add_f32 v[124:125], v[124:125], v[76:77]
	v_pk_add_f32 v[118:119], v[118:119], v[78:79]
	v_pk_add_f32 v[120:121], v[120:121], v[80:81]
	v_pk_add_f32 v[122:123], v[122:123], v[82:83]
	v_pk_add_f32 v[124:125], v[124:125], v[84:85]
	v_pk_add_f32 v[118:119], v[118:119], v[86:87]
	v_pk_add_f32 v[120:121], v[120:121], v[88:89]
	v_pk_add_f32 v[118:119], v[118:119], v[120:121]
	v_pk_add_f32 v[122:123], v[122:123], v[124:125]
	v_add_f32_e32 v126, v21, v23
	v_add_f32_e32 v127, v31, v90
	v_pk_add_f32 v[118:119], v[118:119], v[122:123]
	v_add_f32_e32 v126, v126, v127
	v_add_f32_e32 v20, v118, v119
	v_add_f32_e32 v20, v20, v126
	v_mov_b32_e32 v18, v20
	v_cvt_pk_fp8_f32 v32, v21, v23
	v_cvt_pk_fp8_f32 v33, v26, v27
	v_permlane16_swap_b32_e32 v18, v20
	v_mov_b32_e32 v30, v141
	v_cvt_pk_fp8_f32 v30, v31, v36
	v_add_f32_e32 v18, v20, v18
	v_mov_b32_e32 v19, v18
	v_cvt_pk_fp8_f32 v32, v24, v25 op_sel:[0,0,1]
	v_cvt_pk_fp8_f32 v33, v28, v29 op_sel:[0,0,1]
	v_permlane32_swap_b32_e32 v18, v19
	v_mov_b32_e32 v31, v141
	v_mov_b32_e32 v28, v141
	v_add_f32_e32 v35, v18, v19
	v_mov_b32_e32 v29, v141
	v_mov_b32_e32 v24, v141
	v_mov_b32_e32 v25, v141
	v_mov_b32_e32 v22, v141
	v_mov_b32_e32 v23, v141
	v_mov_b32_e32 v20, v141
	v_mov_b32_e32 v21, v141
	v_mov_b32_e32 v18, v141
	v_mov_b32_e32 v19, v141
	v_mov_b32_e32 v26, v141
	v_mov_b32_e32 v27, v141
	v_cvt_pk_fp8_f32 v31, v39, v40
	v_cvt_pk_fp8_f32 v28, v43, v44
	v_cvt_pk_fp8_f32 v29, v47, v48
	v_cvt_pk_fp8_f32 v24, v51, v52
	v_cvt_pk_fp8_f32 v25, v55, v56
	v_cvt_pk_fp8_f32 v22, v59, v60
	v_cvt_pk_fp8_f32 v23, v63, v64
	v_cvt_pk_fp8_f32 v20, v67, v68
	v_cvt_pk_fp8_f32 v21, v71, v72
	v_cvt_pk_fp8_f32 v18, v75, v76
	v_cvt_pk_fp8_f32 v19, v79, v80
	v_cvt_pk_fp8_f32 v26, v83, v84
	v_cvt_pk_fp8_f32 v27, v87, v88
	v_cvt_pk_fp8_f32 v30, v37, v38 op_sel:[0,0,1]
	v_cvt_pk_fp8_f32 v31, v41, v42 op_sel:[0,0,1]
	v_cvt_pk_fp8_f32 v28, v45, v46 op_sel:[0,0,1]
	v_cvt_pk_fp8_f32 v29, v49, v50 op_sel:[0,0,1]
	v_cvt_pk_fp8_f32 v24, v53, v54 op_sel:[0,0,1]
	v_cvt_pk_fp8_f32 v25, v57, v58 op_sel:[0,0,1]
	v_cvt_pk_fp8_f32 v22, v61, v62 op_sel:[0,0,1]
	v_cvt_pk_fp8_f32 v23, v65, v66 op_sel:[0,0,1]
	v_cvt_pk_fp8_f32 v20, v69, v70 op_sel:[0,0,1]
	v_cvt_pk_fp8_f32 v21, v73, v74 op_sel:[0,0,1]
	v_cvt_pk_fp8_f32 v18, v77, v78 op_sel:[0,0,1]
	v_cvt_pk_fp8_f32 v19, v81, v82 op_sel:[0,0,1]
	v_cvt_pk_fp8_f32 v26, v85, v86 op_sel:[0,0,1]
	v_cvt_pk_fp8_f32 v27, v89, v90 op_sel:[0,0,1]
	s_nop 0
	ds_read_u16 v86, v212 offset:64
	ds_read_u16 v87, v212 offset:80
	ds_read_u16 v88, v212 offset:96
	ds_read_u16 v89, v212 offset:112
	ds_read_u16 v90, v212 offset:128
	ds_read_u16 v91, v212 offset:144
	ds_read_u16 v92, v212 offset:160
	ds_read_u16 v93, v212 offset:176
	ds_read_u16 v94, v212 offset:192
	ds_read_u16 v95, v212 offset:208
	ds_read_u16 v96, v212 offset:224
	ds_read_u16 v97, v212 offset:240
	ds_read_u16 v98, v212 offset:256
	ds_read_u16 v99, v212 offset:272
	ds_read_u16 v100, v212 offset:288
	ds_read_u16 v101, v212 offset:304
	ds_read_u16 v102, v212 offset:320
	ds_read_u16 v103, v212 offset:336
	ds_read_u16 v104, v212 offset:352
	ds_read_u16 v105, v212 offset:368
	ds_read_u16 v106, v212 offset:384
	ds_read_u16 v107, v212 offset:400
	ds_read_u16 v108, v212 offset:416
	ds_read_u16 v109, v212 offset:432
	ds_read_u16 v110, v212 offset:448
	ds_read_u16 v111, v212 offset:464
	ds_read_u16 v112, v212 offset:480
	ds_read_u16 v113, v212 offset:496
	v_ashrrev_i32_e32 v36, 1, v210
	v_cmp_gt_i32_e32 vcc, 4, v36
	v_add_u32_e32 v37, 12, v117
	v_mov_b32_e32 v54, s9
	v_cndmask_b32_e32 v37, v37, v117, vcc
	v_add_u32_e32 v36, v37, v36
	v_and_b32_e32 v37, 15, v36
	v_mad_u32_u24 v37, v37, s24, v54
	v_lshrrev_b32_e32 v36, 4, v36
	v_lshlrev_b32_e32 v54, 3, v210
	v_mul_lo_u32 v36, v36, s8
	v_and_b32_e32 v54, 8, v54
	v_add3_u32 v36, v37, v36, v54
	v_lshrrev_b32_e32 v37, 2, v214
	s_movk_i32 s8, 0xa40
	v_mul_lo_u32 v37, v37, s8
	v_add_u32_e32 v37, s9, v37
	v_and_b32_e32 v54, 48, v116
	v_mul_lo_u32 v55, v213, s24
	v_add3_u32 v37, v37, v54, v55
	s_waitcnt lgkmcnt(0)
	v_lshl_add_u32 v244, v86, 7, v116
	global_load_dwordx4 v[38:41], v244, s[48:49]
	v_lshl_add_u32 v246, v87, 7, v116
	global_load_dwordx4 v[42:45], v246, s[48:49]
	v_lshl_add_u32 v248, v88, 7, v116
	global_load_dwordx4 v[46:49], v248, s[48:49]
	v_lshl_add_u32 v250, v89, 7, v116
	global_load_dwordx4 v[50:53], v250, s[48:49]
	v_lshl_add_u32 v244, v90, 7, v116
	global_load_dwordx4 v[156:159], v244, s[48:49]
	v_lshl_add_u32 v246, v91, 7, v116
	global_load_dwordx4 v[160:163], v246, s[48:49]
	v_lshl_add_u32 v248, v92, 7, v116
	global_load_dwordx4 v[164:167], v248, s[48:49]
	v_lshl_add_u32 v250, v93, 7, v116
	global_load_dwordx4 v[168:171], v250, s[48:49]
	v_lshl_add_u32 v244, v94, 7, v116
	global_load_dwordx4 v[172:175], v244, s[48:49]
	v_lshl_add_u32 v246, v95, 7, v116
	global_load_dwordx4 v[176:179], v246, s[48:49]
	v_lshl_add_u32 v248, v96, 7, v116
	global_load_dwordx4 v[180:183], v248, s[48:49]
	v_lshl_add_u32 v250, v97, 7, v116
	global_load_dwordx4 v[184:187], v250, s[48:49]
	v_lshl_add_u32 v244, v98, 7, v116
	global_load_dwordx4 v[188:191], v244, s[48:49]
	v_lshl_add_u32 v246, v99, 7, v116
	global_load_dwordx4 v[192:195], v246, s[48:49]
	v_lshl_add_u32 v248, v100, 7, v116
	global_load_dwordx4 v[196:199], v248, s[48:49]
	v_lshl_add_u32 v250, v101, 7, v116
	global_load_dwordx4 v[224:227], v250, s[48:49]
	v_lshl_add_u32 v244, v102, 7, v116
	global_load_dwordx4 v[228:231], v244, s[48:49]
	v_lshl_add_u32 v246, v103, 7, v116
	global_load_dwordx4 v[232:235], v246, s[48:49]
	v_lshl_add_u32 v248, v104, 7, v116
	global_load_dwordx4 v[236:239], v248, s[48:49]
	v_lshl_add_u32 v250, v105, 7, v116
	global_load_dwordx4 v[240:243], v250, s[48:49]
	s_waitcnt vmcnt(23)
	ds_write_b128 v37, v[2:5]
	s_waitcnt vmcnt(22)
	ds_write_b128 v37, v[6:9] offset:640
	s_waitcnt vmcnt(21)
	ds_write_b128 v37, v[10:13] offset:1312
	s_waitcnt vmcnt(20)
	ds_write_b128 v37, v[14:17] offset:1952
	v_lshl_add_u32 v244, v106, 7, v116
	global_load_dwordx4 v[2:5], v244, s[48:49]
	v_lshl_add_u32 v246, v107, 7, v116
	global_load_dwordx4 v[6:9], v246, s[48:49]
	v_lshl_add_u32 v248, v108, 7, v116
	global_load_dwordx4 v[10:13], v248, s[48:49]
	v_lshl_add_u32 v250, v109, 7, v116
	global_load_dwordx4 v[14:17], v250, s[48:49]
	s_waitcnt lgkmcnt(0)
	ds_read_b64_tr_b8 v[86:87], v36 offset:0
	ds_read_b64_tr_b8 v[88:89], v36 offset:16
	ds_read_b64_tr_b8 v[90:91], v36 offset:32
	ds_read_b64_tr_b8 v[92:93], v36 offset:48
	ds_read_b64_tr_b8 v[94:95], v36 offset:2624
	ds_read_b64_tr_b8 v[96:97], v36 offset:2640
	ds_read_b64_tr_b8 v[98:99], v36 offset:2656
	ds_read_b64_tr_b8 v[100:101], v36 offset:2672
	s_waitcnt lgkmcnt(0)
	s_waitcnt vmcnt(23)
	ds_write_b128 v37, v[38:41]
	s_waitcnt vmcnt(22)
	ds_write_b128 v37, v[42:45] offset:640
	s_waitcnt vmcnt(21)
	ds_write_b128 v37, v[46:49] offset:1312
	s_waitcnt vmcnt(20)
	ds_write_b128 v37, v[50:53] offset:1952
	v_lshl_add_u32 v244, v110, 7, v116
	global_load_dwordx4 v[38:41], v244, s[48:49]
	v_lshl_add_u32 v246, v111, 7, v116
	global_load_dwordx4 v[42:45], v246, s[48:49]
	v_lshl_add_u32 v248, v112, 7, v116
	global_load_dwordx4 v[46:49], v248, s[48:49]
	v_lshl_add_u32 v250, v113, 7, v116
	global_load_dwordx4 v[50:53], v250, s[48:49]
	s_waitcnt lgkmcnt(0)
	ds_read_b64_tr_b8 v[118:119], v36 offset:0
	ds_read_b64_tr_b8 v[120:121], v36 offset:16
	ds_read_b64_tr_b8 v[122:123], v36 offset:32
	ds_read_b64_tr_b8 v[124:125], v36 offset:48
	ds_read_b64_tr_b8 v[126:127], v36 offset:2624
	ds_read_b64_tr_b8 v[128:129], v36 offset:2640
	ds_read_b64_tr_b8 v[130:131], v36 offset:2656
	ds_read_b64_tr_b8 v[132:133], v36 offset:2672
	v_mfma_f32_16x16x32_fp8_fp8 v[54:57], v[32:33], v[86:87], 0
	v_mfma_f32_16x16x32_fp8_fp8 v[58:61], v[32:33], v[88:89], 0
	v_mfma_f32_16x16x32_fp8_fp8 v[62:65], v[32:33], v[90:91], 0
	v_mfma_f32_16x16x32_fp8_fp8 v[66:69], v[32:33], v[92:93], 0
	s_waitcnt lgkmcnt(0)
	s_waitcnt vmcnt(23)
	ds_write_b128 v37, v[156:159]
	s_waitcnt vmcnt(22)
	ds_write_b128 v37, v[160:163] offset:640
	s_waitcnt vmcnt(21)
	ds_write_b128 v37, v[164:167] offset:1312
	s_waitcnt vmcnt(20)
	ds_write_b128 v37, v[168:171] offset:1952
	v_mfma_f32_16x16x32_fp8_fp8 v[70:73], v[32:33], v[94:95], 0
	v_mfma_f32_16x16x32_fp8_fp8 v[74:77], v[32:33], v[96:97], 0
	v_mfma_f32_16x16x32_fp8_fp8 v[78:81], v[32:33], v[98:99], 0
	v_mfma_f32_16x16x32_fp8_fp8 v[82:85], v[32:33], v[100:101], 0
	s_waitcnt lgkmcnt(0)
	ds_read_b64_tr_b8 v[86:87], v36 offset:0
	ds_read_b64_tr_b8 v[88:89], v36 offset:16
	ds_read_b64_tr_b8 v[90:91], v36 offset:32
	ds_read_b64_tr_b8 v[92:93], v36 offset:48
	ds_read_b64_tr_b8 v[94:95], v36 offset:2624
	ds_read_b64_tr_b8 v[96:97], v36 offset:2640
	ds_read_b64_tr_b8 v[98:99], v36 offset:2656
	ds_read_b64_tr_b8 v[100:101], v36 offset:2672
	v_mfma_f32_16x16x32_fp8_fp8 v[54:57], v[30:31], v[118:119], v[54:57]
	v_mfma_f32_16x16x32_fp8_fp8 v[58:61], v[30:31], v[120:121], v[58:61]
	v_mfma_f32_16x16x32_fp8_fp8 v[62:65], v[30:31], v[122:123], v[62:65]
	v_mfma_f32_16x16x32_fp8_fp8 v[66:69], v[30:31], v[124:125], v[66:69]
	s_waitcnt lgkmcnt(0)
	s_waitcnt vmcnt(19)
	ds_write_b128 v37, v[172:175]
	s_waitcnt vmcnt(18)
	ds_write_b128 v37, v[176:179] offset:640
	s_waitcnt vmcnt(17)
	ds_write_b128 v37, v[180:183] offset:1312
	s_waitcnt vmcnt(16)
	ds_write_b128 v37, v[184:187] offset:1952
	v_mfma_f32_16x16x32_fp8_fp8 v[70:73], v[30:31], v[126:127], v[70:73]
	v_mfma_f32_16x16x32_fp8_fp8 v[74:77], v[30:31], v[128:129], v[74:77]
	v_mfma_f32_16x16x32_fp8_fp8 v[78:81], v[30:31], v[130:131], v[78:81]
	v_mfma_f32_16x16x32_fp8_fp8 v[82:85], v[30:31], v[132:133], v[82:85]
	s_waitcnt lgkmcnt(0)
	ds_read_b64_tr_b8 v[118:119], v36 offset:0
	ds_read_b64_tr_b8 v[120:121], v36 offset:16
	ds_read_b64_tr_b8 v[122:123], v36 offset:32
	ds_read_b64_tr_b8 v[124:125], v36 offset:48
	ds_read_b64_tr_b8 v[126:127], v36 offset:2624
	ds_read_b64_tr_b8 v[128:129], v36 offset:2640
	ds_read_b64_tr_b8 v[130:131], v36 offset:2656
	ds_read_b64_tr_b8 v[132:133], v36 offset:2672
	v_mfma_f32_16x16x32_fp8_fp8 v[54:57], v[28:29], v[86:87], v[54:57]
	v_mfma_f32_16x16x32_fp8_fp8 v[58:61], v[28:29], v[88:89], v[58:61]
	v_mfma_f32_16x16x32_fp8_fp8 v[62:65], v[28:29], v[90:91], v[62:65]
	v_mfma_f32_16x16x32_fp8_fp8 v[66:69], v[28:29], v[92:93], v[66:69]
	s_waitcnt lgkmcnt(0)
	s_waitcnt vmcnt(15)
	ds_write_b128 v37, v[188:191]
	s_waitcnt vmcnt(14)
	ds_write_b128 v37, v[192:195] offset:640
	s_waitcnt vmcnt(13)
	ds_write_b128 v37, v[196:199] offset:1312
	s_waitcnt vmcnt(12)
	ds_write_b128 v37, v[224:227] offset:1952
	v_mfma_f32_16x16x32_fp8_fp8 v[70:73], v[28:29], v[94:95], v[70:73]
	v_mfma_f32_16x16x32_fp8_fp8 v[74:77], v[28:29], v[96:97], v[74:77]
	v_mfma_f32_16x16x32_fp8_fp8 v[78:81], v[28:29], v[98:99], v[78:81]
	v_mfma_f32_16x16x32_fp8_fp8 v[82:85], v[28:29], v[100:101], v[82:85]
	s_waitcnt lgkmcnt(0)
	ds_read_b64_tr_b8 v[86:87], v36 offset:0
	ds_read_b64_tr_b8 v[88:89], v36 offset:16
	ds_read_b64_tr_b8 v[90:91], v36 offset:32
	ds_read_b64_tr_b8 v[92:93], v36 offset:48
	ds_read_b64_tr_b8 v[94:95], v36 offset:2624
	ds_read_b64_tr_b8 v[96:97], v36 offset:2640
	ds_read_b64_tr_b8 v[98:99], v36 offset:2656
	ds_read_b64_tr_b8 v[100:101], v36 offset:2672
	v_mfma_f32_16x16x32_fp8_fp8 v[54:57], v[24:25], v[118:119], v[54:57]
	v_mfma_f32_16x16x32_fp8_fp8 v[58:61], v[24:25], v[120:121], v[58:61]
	v_mfma_f32_16x16x32_fp8_fp8 v[62:65], v[24:25], v[122:123], v[62:65]
	v_mfma_f32_16x16x32_fp8_fp8 v[66:69], v[24:25], v[124:125], v[66:69]
	s_waitcnt lgkmcnt(0)
	s_waitcnt vmcnt(11)
	ds_write_b128 v37, v[228:231]
	s_waitcnt vmcnt(10)
	ds_write_b128 v37, v[232:235] offset:640
	s_waitcnt vmcnt(9)
	ds_write_b128 v37, v[236:239] offset:1312
	s_waitcnt vmcnt(8)
	ds_write_b128 v37, v[240:243] offset:1952
	v_mfma_f32_16x16x32_fp8_fp8 v[70:73], v[24:25], v[126:127], v[70:73]
	v_mfma_f32_16x16x32_fp8_fp8 v[74:77], v[24:25], v[128:129], v[74:77]
	v_mfma_f32_16x16x32_fp8_fp8 v[78:81], v[24:25], v[130:131], v[78:81]
	v_mfma_f32_16x16x32_fp8_fp8 v[82:85], v[24:25], v[132:133], v[82:85]
	s_waitcnt lgkmcnt(0)
	ds_read_b64_tr_b8 v[118:119], v36 offset:0
	ds_read_b64_tr_b8 v[120:121], v36 offset:16
	ds_read_b64_tr_b8 v[122:123], v36 offset:32
	ds_read_b64_tr_b8 v[124:125], v36 offset:48
	ds_read_b64_tr_b8 v[126:127], v36 offset:2624
	ds_read_b64_tr_b8 v[128:129], v36 offset:2640
	ds_read_b64_tr_b8 v[130:131], v36 offset:2656
	ds_read_b64_tr_b8 v[132:133], v36 offset:2672
	v_mfma_f32_16x16x32_fp8_fp8 v[54:57], v[22:23], v[86:87], v[54:57]
	v_mfma_f32_16x16x32_fp8_fp8 v[58:61], v[22:23], v[88:89], v[58:61]
	v_mfma_f32_16x16x32_fp8_fp8 v[62:65], v[22:23], v[90:91], v[62:65]
	v_mfma_f32_16x16x32_fp8_fp8 v[66:69], v[22:23], v[92:93], v[66:69]
	s_waitcnt lgkmcnt(0)
	s_waitcnt vmcnt(7)
	ds_write_b128 v37, v[2:5]
	s_waitcnt vmcnt(6)
	ds_write_b128 v37, v[6:9] offset:640
	s_waitcnt vmcnt(5)
	ds_write_b128 v37, v[10:13] offset:1312
	s_waitcnt vmcnt(4)
	ds_write_b128 v37, v[14:17] offset:1952
	v_mfma_f32_16x16x32_fp8_fp8 v[70:73], v[22:23], v[94:95], v[70:73]
	v_mfma_f32_16x16x32_fp8_fp8 v[74:77], v[22:23], v[96:97], v[74:77]
	v_mfma_f32_16x16x32_fp8_fp8 v[78:81], v[22:23], v[98:99], v[78:81]
	v_mfma_f32_16x16x32_fp8_fp8 v[82:85], v[22:23], v[100:101], v[82:85]
	s_waitcnt lgkmcnt(0)
	ds_read_b64_tr_b8 v[86:87], v36 offset:0
	ds_read_b64_tr_b8 v[88:89], v36 offset:16
	ds_read_b64_tr_b8 v[90:91], v36 offset:32
	ds_read_b64_tr_b8 v[92:93], v36 offset:48
	ds_read_b64_tr_b8 v[94:95], v36 offset:2624
	ds_read_b64_tr_b8 v[96:97], v36 offset:2640
	ds_read_b64_tr_b8 v[98:99], v36 offset:2656
	ds_read_b64_tr_b8 v[100:101], v36 offset:2672
	v_mfma_f32_16x16x32_fp8_fp8 v[54:57], v[20:21], v[118:119], v[54:57]
	v_mfma_f32_16x16x32_fp8_fp8 v[58:61], v[20:21], v[120:121], v[58:61]
	v_mfma_f32_16x16x32_fp8_fp8 v[62:65], v[20:21], v[122:123], v[62:65]
	v_mfma_f32_16x16x32_fp8_fp8 v[66:69], v[20:21], v[124:125], v[66:69]
	s_waitcnt lgkmcnt(0)
	s_waitcnt vmcnt(3)
	ds_write_b128 v37, v[38:41]
	s_waitcnt vmcnt(2)
	ds_write_b128 v37, v[42:45] offset:640
	s_waitcnt vmcnt(1)
	ds_write_b128 v37, v[46:49] offset:1312
	s_waitcnt vmcnt(0)
	ds_write_b128 v37, v[50:53] offset:1952
	v_mfma_f32_16x16x32_fp8_fp8 v[70:73], v[20:21], v[126:127], v[70:73]
	v_mfma_f32_16x16x32_fp8_fp8 v[74:77], v[20:21], v[128:129], v[74:77]
	v_mfma_f32_16x16x32_fp8_fp8 v[78:81], v[20:21], v[130:131], v[78:81]
	v_mfma_f32_16x16x32_fp8_fp8 v[82:85], v[20:21], v[132:133], v[82:85]
	s_waitcnt lgkmcnt(0)
	ds_read_b64_tr_b8 v[118:119], v36 offset:0
	ds_read_b64_tr_b8 v[120:121], v36 offset:16
	ds_read_b64_tr_b8 v[122:123], v36 offset:32
	ds_read_b64_tr_b8 v[124:125], v36 offset:48
	ds_read_b64_tr_b8 v[126:127], v36 offset:2624
	ds_read_b64_tr_b8 v[128:129], v36 offset:2640
	ds_read_b64_tr_b8 v[130:131], v36 offset:2656
	ds_read_b64_tr_b8 v[132:133], v36 offset:2672
	v_mfma_f32_16x16x32_fp8_fp8 v[54:57], v[18:19], v[86:87], v[54:57]
	v_mfma_f32_16x16x32_fp8_fp8 v[58:61], v[18:19], v[88:89], v[58:61]
	v_mfma_f32_16x16x32_fp8_fp8 v[62:65], v[18:19], v[90:91], v[62:65]
	v_mfma_f32_16x16x32_fp8_fp8 v[66:69], v[18:19], v[92:93], v[66:69]
	s_waitcnt lgkmcnt(0)
	v_mfma_f32_16x16x32_fp8_fp8 v[70:73], v[18:19], v[94:95], v[70:73]
	v_mfma_f32_16x16x32_fp8_fp8 v[74:77], v[18:19], v[96:97], v[74:77]
	v_mfma_f32_16x16x32_fp8_fp8 v[78:81], v[18:19], v[98:99], v[78:81]
	v_mfma_f32_16x16x32_fp8_fp8 v[82:85], v[18:19], v[100:101], v[82:85]
	v_mfma_f32_16x16x32_fp8_fp8 v[2:5], v[26:27], v[118:119], v[54:57]
	v_mfma_f32_16x16x32_fp8_fp8 v[6:9], v[26:27], v[120:121], v[58:61]
	v_mfma_f32_16x16x32_fp8_fp8 v[10:13], v[26:27], v[122:123], v[62:65]
	v_mfma_f32_16x16x32_fp8_fp8 v[14:17], v[26:27], v[124:125], v[66:69]
	v_mfma_f32_16x16x32_fp8_fp8 v[18:21], v[26:27], v[126:127], v[70:73]
	v_mfma_f32_16x16x32_fp8_fp8 v[22:25], v[26:27], v[128:129], v[74:77]
	v_mfma_f32_16x16x32_fp8_fp8 v[30:33], v[26:27], v[130:131], v[78:81]
	v_mfma_f32_16x16x32_fp8_fp8 v[26:29], v[26:27], v[132:133], v[82:85]
	v_div_scale_f32 v36, s[8:9], v35, v35, 1.0
	v_rcp_f32_e32 v37, v36
	v_readlane_b32 s8, v254, 62
	s_add_u32 s0, s8, s0
	v_readlane_b32 s8, v254, 63
	s_addc_u32 s1, s8, s1
	v_cmp_gt_i32_e64 s[8:9], 2, v211
	v_fma_f32 v38, -v36, v37, 1.0
	v_fmac_f32_e32 v37, v38, v37
	v_div_scale_f32 v38, vcc, 1.0, v35, 1.0
	v_mul_f32_e32 v39, v38, v37
	v_fma_f32 v40, -v36, v39, v38
	v_fmac_f32_e32 v39, v40, v37
	v_fma_f32 v36, -v36, v39, v38
	v_div_fmas_f32 v36, v36, v37, v39
	v_div_fixup_f32 v35, v36, v35, 1.0
	ds_bpermute_b32 v36, v34, v35
	ds_bpermute_b32 v37, v34, v35 offset:16
	v_cmp_eq_u32_e32 vcc, 0, v211
	s_and_saveexec_b64 s[10:11], s[8:9]
	s_cbranch_execz .LBB0_1336
	v_lshl_add_u32 v38, v211, 8, v210
	v_cndmask_b32_e32 v2, v18, v2, vcc
	s_waitcnt lgkmcnt(0)
	v_cndmask_b32_e32 v18, v37, v36, vcc
	v_mul_f32_e32 v2, v2, v18
	v_ashrrev_i32_e32 v39, 31, v38
	v_cvt_pk_bf16_f32 v2, v2, s0
	v_lshl_add_u64 v[36:37], v[38:39], 1, s[0:1]
	global_store_short v[36:37], v2, off
	v_cndmask_b32_e32 v2, v22, v6, vcc
	v_mul_f32_e32 v2, v2, v18
	v_cvt_pk_bf16_f32 v2, v2, s0
	global_store_short v[36:37], v2, off offset:32
	v_cndmask_b32_e32 v2, v30, v10, vcc
	v_mul_f32_e32 v2, v2, v18
	v_cvt_pk_bf16_f32 v2, v2, s0
	global_store_short v[36:37], v2, off offset:64
	v_cndmask_b32_e32 v2, v26, v14, vcc
	v_mul_f32_e32 v2, v2, v18
	v_cvt_pk_bf16_f32 v2, v2, s0
	global_store_short v[36:37], v2, off offset:96
